# speedup vs baseline: 1.0083x; 1.0033x over previous
.LBB2_9:
	s_lshr_b32 s8, s14, 7
	v_and_b32_e32 v1, 15, v0
	v_bfe_u32 v98, v0, 4, 2
	s_bfe_u32 s9, s14, 0x10006
	s_and_b64 vcc, exec, s[4:5]
	s_cbranch_vccz .LBB2_13
	s_barrier
	s_cmp_lt_i32 s6, 64
	s_mov_b32 s4, 0
	s_cbranch_scc1 .LBB2_41
	v_lshrrev_b32_e32 v2, 1, v0
	v_bfe_u32 v3, v0, 1, 3
	v_bitop3_b32 v2, v98, v2, 7 bitop3:0x78
	s_mul_i32 s5, s9, 0x60
	v_lshlrev_b32_e32 v99, 4, v2
	v_bitop3_b32 v2, v98, v3, 4 bitop3:0x36
	v_or_b32_e32 v4, s5, v1
	v_lshlrev_b32_e32 v102, 4, v2
	v_mov_b32_e32 v2, 0
	s_lshl_b32 s5, s8, 13
	v_lshlrev_b32_e32 v100, 7, v1
	v_lshlrev_b32_e32 v101, 7, v4
	v_mov_b32_e32 v3, v2
	v_mov_b32_e32 v4, v2
	v_mov_b32_e32 v5, v2
	v_mov_b32_e32 v6, v2
	v_mov_b32_e32 v7, v2
	v_mov_b32_e32 v8, v2
	v_mov_b32_e32 v9, v2
	v_mov_b32_e32 v34, v2
	v_mov_b32_e32 v35, v2
	v_mov_b32_e32 v36, v2
	v_mov_b32_e32 v37, v2
	v_mov_b32_e32 v38, v2
	v_mov_b32_e32 v39, v2
	v_mov_b32_e32 v40, v2
	v_mov_b32_e32 v41, v2
	v_mov_b32_e32 v66, v2
	v_mov_b32_e32 v67, v2
	v_mov_b32_e32 v68, v2
	v_mov_b32_e32 v69, v2
	v_mov_b32_e32 v70, v2
	v_mov_b32_e32 v71, v2
	v_mov_b32_e32 v72, v2
	v_mov_b32_e32 v73, v2
	v_mov_b32_e32 v10, v2
	v_mov_b32_e32 v11, v2
	v_mov_b32_e32 v12, v2
	v_mov_b32_e32 v13, v2
	v_mov_b32_e32 v14, v2
	v_mov_b32_e32 v15, v2
	v_mov_b32_e32 v16, v2
	v_mov_b32_e32 v17, v2
	v_mov_b32_e32 v42, v2
	v_mov_b32_e32 v43, v2
	v_mov_b32_e32 v44, v2
	v_mov_b32_e32 v45, v2
	v_mov_b32_e32 v46, v2
	v_mov_b32_e32 v47, v2
	v_mov_b32_e32 v48, v2
	v_mov_b32_e32 v49, v2
	v_mov_b32_e32 v74, v2
	v_mov_b32_e32 v75, v2
	v_mov_b32_e32 v76, v2
	v_mov_b32_e32 v77, v2
	v_mov_b32_e32 v78, v2
	v_mov_b32_e32 v79, v2
	v_mov_b32_e32 v80, v2
	v_mov_b32_e32 v81, v2
	v_mov_b32_e32 v18, v2
	v_mov_b32_e32 v19, v2
	v_mov_b32_e32 v20, v2
	v_mov_b32_e32 v21, v2
	v_mov_b32_e32 v22, v2
	v_mov_b32_e32 v23, v2
	v_mov_b32_e32 v24, v2
	v_mov_b32_e32 v25, v2
	v_mov_b32_e32 v50, v2
	v_mov_b32_e32 v51, v2
	v_mov_b32_e32 v52, v2
	v_mov_b32_e32 v53, v2
	v_mov_b32_e32 v54, v2
	v_mov_b32_e32 v55, v2
	v_mov_b32_e32 v56, v2
	v_mov_b32_e32 v57, v2
	v_mov_b32_e32 v82, v2
	v_mov_b32_e32 v83, v2
	v_mov_b32_e32 v84, v2
	v_mov_b32_e32 v85, v2
	v_mov_b32_e32 v86, v2
	v_mov_b32_e32 v87, v2
	v_mov_b32_e32 v88, v2
	v_mov_b32_e32 v89, v2
	v_mov_b32_e32 v26, v2
	v_mov_b32_e32 v27, v2
	v_mov_b32_e32 v28, v2
	v_mov_b32_e32 v29, v2
	v_mov_b32_e32 v30, v2
	v_mov_b32_e32 v31, v2
	v_mov_b32_e32 v32, v2
	v_mov_b32_e32 v33, v2
	v_mov_b32_e32 v58, v2
	v_mov_b32_e32 v59, v2
	v_mov_b32_e32 v60, v2
	v_mov_b32_e32 v61, v2
	v_mov_b32_e32 v62, v2
	v_mov_b32_e32 v63, v2
	v_mov_b32_e32 v64, v2
	v_mov_b32_e32 v65, v2
	v_mov_b32_e32 v90, v2
	v_mov_b32_e32 v91, v2
	v_mov_b32_e32 v92, v2
	v_mov_b32_e32 v93, v2
	v_mov_b32_e32 v94, v2
	v_mov_b32_e32 v95, v2
	v_mov_b32_e32 v96, v2
	v_mov_b32_e32 v97, v2
	v_add3_u32 v137, v99, s5, v100
	v_add_u32_e32 v138, v99, v101
	v_add3_u32 v139, v102, s5, v100
	v_add_u32_e32 v140, v102, v101
	s_mov_b32 s20, 0
	.p2align	6
.LBB2_12:
	s_mul_i32 s6, s4, 0x6000
	s_add_i32 s6, s6, 0x10000
	v_add_u32_e32 v136, s20, v137
	v_add_u32_e32 v103, s6, v138
	ds_read_b128 v[104:107], v103 offset:32768
	ds_read_b128 v[108:111], v103 offset:34816
	ds_read_b128 v[112:115], v136
	ds_read_b128 v[116:119], v136 offset:2048
	ds_read_b128 v[120:123], v103 offset:36864
	ds_read_b128 v[124:127], v103 offset:38912
	ds_read_b128 v[128:131], v103 offset:40960
	ds_read_b128 v[132:135], v103 offset:43008
	s_waitcnt lgkmcnt(0)
	v_mfma_f32_16x16x32_f16 v[94:97], v[104:107], v[112:115], v[94:97]
	v_add_u32_e32 v103, s6, v140
	v_mfma_f32_16x16x32_f16 v[90:93], v[108:111], v[112:115], v[90:93]
	v_mfma_f32_16x16x32_f16 v[62:65], v[120:123], v[112:115], v[62:65]
	v_mfma_f32_16x16x32_f16 v[58:61], v[124:127], v[112:115], v[58:61]
	v_mfma_f32_16x16x32_f16 v[30:33], v[128:131], v[112:115], v[30:33]
	v_mfma_f32_16x16x32_f16 v[26:29], v[132:135], v[112:115], v[26:29]
	v_mfma_f32_16x16x32_f16 v[86:89], v[104:107], v[116:119], v[86:89]
	v_mfma_f32_16x16x32_f16 v[82:85], v[108:111], v[116:119], v[82:85]
	v_mfma_f32_16x16x32_f16 v[54:57], v[120:123], v[116:119], v[54:57]
	v_mfma_f32_16x16x32_f16 v[50:53], v[124:127], v[116:119], v[50:53]
	v_mfma_f32_16x16x32_f16 v[22:25], v[128:131], v[116:119], v[22:25]
	v_mfma_f32_16x16x32_f16 v[18:21], v[132:135], v[116:119], v[18:21]
	ds_read_b128 v[112:115], v136 offset:4096
	ds_read_b128 v[116:119], v136 offset:6144
	v_add_u32_e32 v136, s20, v139
	s_waitcnt lgkmcnt(0)
	v_mfma_f32_16x16x32_f16 v[78:81], v[104:107], v[112:115], v[78:81]
	v_mfma_f32_16x16x32_f16 v[74:77], v[108:111], v[112:115], v[74:77]
	v_mfma_f32_16x16x32_f16 v[46:49], v[120:123], v[112:115], v[46:49]
	v_mfma_f32_16x16x32_f16 v[42:45], v[124:127], v[112:115], v[42:45]
	v_mfma_f32_16x16x32_f16 v[14:17], v[128:131], v[112:115], v[14:17]
	v_mfma_f32_16x16x32_f16 v[10:13], v[132:135], v[112:115], v[10:13]
	v_mfma_f32_16x16x32_f16 v[70:73], v[104:107], v[116:119], v[70:73]
	v_mfma_f32_16x16x32_f16 v[66:69], v[108:111], v[116:119], v[66:69]
	ds_read_b128 v[104:107], v103 offset:32768
	ds_read_b128 v[108:111], v103 offset:34816
	v_mfma_f32_16x16x32_f16 v[38:41], v[120:123], v[116:119], v[38:41]
	v_mfma_f32_16x16x32_f16 v[34:37], v[124:127], v[116:119], v[34:37]
	v_mfma_f32_16x16x32_f16 v[6:9], v[128:131], v[116:119], v[6:9]
	v_mfma_f32_16x16x32_f16 v[2:5], v[132:135], v[116:119], v[2:5]
	ds_read_b128 v[112:115], v136
	ds_read_b128 v[116:119], v136 offset:2048
	ds_read_b128 v[120:123], v103 offset:36864
	ds_read_b128 v[124:127], v103 offset:38912
	ds_read_b128 v[128:131], v103 offset:40960
	ds_read_b128 v[132:135], v103 offset:43008
	s_waitcnt lgkmcnt(0)
	v_mfma_f32_16x16x32_f16 v[94:97], v[104:107], v[112:115], v[94:97]
	v_mfma_f32_16x16x32_f16 v[90:93], v[108:111], v[112:115], v[90:93]
	v_mfma_f32_16x16x32_f16 v[62:65], v[120:123], v[112:115], v[62:65]
	v_mfma_f32_16x16x32_f16 v[58:61], v[124:127], v[112:115], v[58:61]
	v_mfma_f32_16x16x32_f16 v[30:33], v[128:131], v[112:115], v[30:33]
	v_mfma_f32_16x16x32_f16 v[26:29], v[132:135], v[112:115], v[26:29]
	v_mfma_f32_16x16x32_f16 v[86:89], v[104:107], v[116:119], v[86:89]
	v_mfma_f32_16x16x32_f16 v[82:85], v[108:111], v[116:119], v[82:85]
	v_mfma_f32_16x16x32_f16 v[54:57], v[120:123], v[116:119], v[54:57]
	v_mfma_f32_16x16x32_f16 v[50:53], v[124:127], v[116:119], v[50:53]
	v_mfma_f32_16x16x32_f16 v[22:25], v[128:131], v[116:119], v[22:25]
	v_mfma_f32_16x16x32_f16 v[18:21], v[132:135], v[116:119], v[18:21]
	ds_read_b128 v[112:115], v136 offset:4096
	ds_read_b128 v[116:119], v136 offset:6144
	s_waitcnt lgkmcnt(0)
	s_barrier
	s_waitcnt lgkmcnt(0)
	v_mfma_f32_16x16x32_f16 v[78:81], v[104:107], v[112:115], v[78:81]
	v_mfma_f32_16x16x32_f16 v[74:77], v[108:111], v[112:115], v[74:77]
	v_mfma_f32_16x16x32_f16 v[46:49], v[120:123], v[112:115], v[46:49]
	v_mfma_f32_16x16x32_f16 v[42:45], v[124:127], v[112:115], v[42:45]
	v_mfma_f32_16x16x32_f16 v[14:17], v[128:131], v[112:115], v[14:17]
	v_mfma_f32_16x16x32_f16 v[10:13], v[132:135], v[112:115], v[10:13]
	v_mfma_f32_16x16x32_f16 v[70:73], v[104:107], v[116:119], v[70:73]
	v_mfma_f32_16x16x32_f16 v[66:69], v[108:111], v[116:119], v[66:69]
	v_mfma_f32_16x16x32_f16 v[38:41], v[120:123], v[116:119], v[38:41]
	v_mfma_f32_16x16x32_f16 v[34:37], v[124:127], v[116:119], v[34:37]
	v_mfma_f32_16x16x32_f16 v[6:9], v[128:131], v[116:119], v[6:9]
	v_mfma_f32_16x16x32_f16 v[2:5], v[132:135], v[116:119], v[2:5]
	s_add_i32 s4, s4, 1
	s_cmp_lg_u32 s4, 2
	s_cselect_b32 s4, s4, 0
	s_add_i32 s20, s20, 0x8000
	s_cmp_lg_u32 s20, 0x18000
	s_cselect_b32 s20, s20, 0
	s_add_i32 s7, s7, -1
	s_cmp_lg_u32 s7, 0
	s_cbranch_scc1 .LBB2_12
	s_branch .LBB2_14

	.amdhsa_kernel _Z7gemm_dbILi256ELi192ELi64ELi96ELi64ELi2ELi1ELi4EEvPKDF16_S1_PfPDF16_S3_S3_PK15HIP_vector_typeIfLj2EEiii
		.amdhsa_group_segment_fixed_size 32768
		.amdhsa_private_segment_fixed_size 0
		.amdhsa_kernarg_size 68
		.amdhsa_user_sgpr_count 2
		.amdhsa_user_sgpr_dispatch_ptr 0
		.amdhsa_user_sgpr_queue_ptr 0
		.amdhsa_user_sgpr_kernarg_segment_ptr 1
		.amdhsa_user_sgpr_dispatch_id 0
		.amdhsa_user_sgpr_kernarg_preload_length 0
		.amdhsa_user_sgpr_kernarg_preload_offset 0
		.amdhsa_user_sgpr_private_segment_size 0
		.amdhsa_uses_dynamic_stack 0
		.amdhsa_enable_private_segment 0
		.amdhsa_system_sgpr_workgroup_id_x 1
		.amdhsa_system_sgpr_workgroup_id_y 0
		.amdhsa_system_sgpr_workgroup_id_z 0
		.amdhsa_system_sgpr_workgroup_info 0
		.amdhsa_system_vgpr_workitem_id 0
		.amdhsa_next_free_vgpr 141
		.amdhsa_next_free_sgpr 21
		.amdhsa_accum_offset 144
		.amdhsa_reserve_vcc 1
		.amdhsa_float_round_mode_32 0
		.amdhsa_float_round_mode_16_64 0
		.amdhsa_float_denorm_mode_32 3
		.amdhsa_float_denorm_mode_16_64 3
		.amdhsa_dx10_clamp 1
		.amdhsa_ieee_mode 1
		.amdhsa_fp16_overflow 0
		.amdhsa_tg_split 0
		.amdhsa_exception_fp_ieee_invalid_op 0
		.amdhsa_exception_fp_denorm_src 0
		.amdhsa_exception_fp_ieee_div_zero 0
		.amdhsa_exception_fp_ieee_overflow 0
		.amdhsa_exception_fp_ieee_underflow 0
		.amdhsa_exception_fp_ieee_inexact 0
		.amdhsa_exception_int_div_zero 0
	.end_amdhsa_kernel

_Z7gemm_dbILi128ELi128ELi64ELi64ELi64ELi3ELi0ELi4EEvPKDF16_S1_PfPDF16_S3_S3_PK15HIP_vector_typeIfLj2EEiii:
	s_load_dwordx4 s[4:7], s[0:1], 0x38
	s_and_b32 s10, s2, 7
	s_lshr_b32 s2, s2, 3
	s_waitcnt lgkmcnt(0)
	v_readfirstlane_b32 s7, v0
	s_ashr_i32 s3, s5, 31
	s_lshr_b32 s3, s3, 25
	s_add_i32 s3, s5, s3
	s_ashr_i32 s8, s3, 7
	s_abs_i32 s9, s8
	v_cvt_f32_u32_e32 v1, s9
	s_ashr_i32 s11, s4, 31
	s_lshr_b32 s11, s11, 22
	s_add_i32 s4, s4, s11
	v_rcp_iflag_f32_e32 v1, v1
	s_ashr_i32 s4, s4, 10
	s_mul_i32 s4, s4, s10
	s_sub_i32 s10, 0, s9
	v_mul_f32_e32 v1, 0x4f7ffffe, v1
	v_cvt_u32_f32_e32 v1, v1
	s_ashr_i32 s3, s3, 31
	v_readfirstlane_b32 s11, v1
	s_mul_i32 s10, s10, s11
	s_mul_hi_u32 s10, s11, s10
	s_add_i32 s11, s11, s10
	s_mul_hi_u32 s10, s2, s11
	s_mul_i32 s11, s10, s9
	s_sub_i32 s11, s2, s11
	s_add_i32 s12, s10, 1
	s_sub_i32 s13, s11, s9
	s_cmp_ge_u32 s11, s9
	s_cselect_b32 s10, s12, s10
	s_cselect_b32 s11, s13, s11
	s_add_i32 s12, s10, 1
	s_cmp_ge_u32 s11, s9
	s_cselect_b32 s9, s12, s10
	s_xor_b32 s9, s9, s3
	s_sub_i32 s3, s9, s3
	s_add_i32 s4, s3, s4
	s_mul_i32 s3, s3, s8
	s_sub_i32 s2, s2, s3
	s_ashr_i32 s3, s6, 31
	s_lshr_b32 s3, s3, 26
	s_add_i32 s3, s6, s3
	s_lshl_b32 s4, s4, 7
	s_lshl_b32 s2, s2, 7
	s_ashr_i32 s14, s3, 6
	s_cmpk_lt_u32 s7, 0x100
	s_cselect_b64 s[8:9], -1, 0
	s_mov_b64 s[10:11], -1
	s_and_b64 vcc, exec, s[8:9]
	s_cbranch_vccnz .LBB3_9
	v_add_u32_e32 v1, 0xffffff00, v0
	s_load_dwordx4 s[16:19], s[0:1], 0x0
	v_lshlrev_b32_e32 v20, 4, v1
	v_ashrrev_i32_e32 v10, 3, v1
	v_lshrrev_b32_e32 v1, 4, v1
	v_xor_b32_e32 v1, v1, v0
	v_lshlrev_b32_e32 v1, 4, v1
	v_and_b32_e32 v16, 0x70, v1
	v_add_u32_e32 v1, 0x1000, v20
	v_lshrrev_b32_e32 v1, 7, v1
	v_add_u32_e32 v6, 0x2000, v20
	s_movk_i32 s3, 0x880
	v_add_u32_e32 v4, s4, v1
	v_lshrrev_b32_e32 v14, 7, v6
	v_add_u32_e32 v11, 0x3000, v20
	s_waitcnt lgkmcnt(0)
	v_mov_b64_e32 v[18:19], s[18:19]
	v_add_u32_e32 v1, s2, v1
	v_lshrrev_b32_e32 v21, 7, v11
	v_mad_u64_u32 v[12:13], s[10:11], v1, s3, v[18:19]
	v_add_u32_e32 v1, s2, v14
	v_add_u32_e32 v2, s4, v10
	v_mov_b64_e32 v[8:9], s[16:17]
	v_add_u32_e32 v6, s4, v14
	v_add_u32_e32 v11, s4, v21
	v_add_u32_e32 v10, s2, v10
	v_mad_u64_u32 v[14:15], s[10:11], v1, s3, v[18:19]
	v_add_u32_e32 v1, s2, v21
	v_mad_i64_i32 v[2:3], s[10:11], v2, s3, v[8:9]
	v_mov_b32_e32 v17, 0
	v_mad_i64_i32 v[4:5], s[10:11], v4, s3, v[8:9]
	v_mad_i64_i32 v[6:7], s[10:11], v6, s3, v[8:9]
	v_mad_i64_i32 v[8:9], s[10:11], v11, s3, v[8:9]
	v_mad_i64_i32 v[10:11], s[10:11], v10, s3, v[18:19]
	v_mad_u64_u32 v[18:19], s[10:11], v1, s3, v[18:19]
	v_add_u32_e32 v1, 0, v20
	v_lshl_add_u64 v[2:3], v[2:3], 0, v[16:17]
	v_lshl_add_u64 v[4:5], v[4:5], 0, v[16:17]
	v_lshl_add_u64 v[6:7], v[6:7], 0, v[16:17]
	v_lshl_add_u64 v[8:9], v[8:9], 0, v[16:17]
	v_lshl_add_u64 v[10:11], v[10:11], 0, v[16:17]
	v_lshl_add_u64 v[12:13], v[12:13], 0, v[16:17]
	v_lshl_add_u64 v[14:15], v[14:15], 0, v[16:17]
	v_lshl_add_u64 v[16:17], v[18:19], 0, v[16:17]
	v_readfirstlane_b32 s3, v1
	v_add_u32_e32 v18, 0x1000, v1
	s_mov_b32 m0, s3
	v_readfirstlane_b32 s3, v18
	v_add_u32_e32 v18, 0x2000, v1
	global_load_lds_dwordx4 v[2:3], off
	s_mov_b32 m0, s3
	v_readfirstlane_b32 s3, v18
	v_add_u32_e32 v18, 0x3000, v1
	global_load_lds_dwordx4 v[4:5], off
	s_mov_b32 m0, s3
	v_readfirstlane_b32 s3, v18
	v_add_u32_e32 v18, 0x4000, v1
	global_load_lds_dwordx4 v[6:7], off
	s_mov_b32 m0, s3
	v_readfirstlane_b32 s3, v18
	v_add_u32_e32 v18, 0x5000, v1
	global_load_lds_dwordx4 v[8:9], off
	s_mov_b32 m0, s3
	v_readfirstlane_b32 s3, v18
	v_add_u32_e32 v18, 0x6000, v1
	global_load_lds_dwordx4 v[10:11], off
	s_mov_b32 m0, s3
	v_readfirstlane_b32 s3, v18
	v_add_u32_e32 v18, 0x7000, v1
	global_load_lds_dwordx4 v[12:13], off
	s_mov_b32 m0, s3
	v_readfirstlane_b32 s3, v18
	v_add_u32_e32 v20, 0x8000, v1
	global_load_lds_dwordx4 v[14:15], off
	s_mov_b32 m0, s3
	s_mov_b64 s[10:11], 0x80
	v_readfirstlane_b32 s3, v20
	v_add_u32_e32 v20, 0x9000, v1
	global_load_lds_dwordx4 v[16:17], off
	v_lshl_add_u64 v[18:19], v[2:3], 0, s[10:11]
	s_mov_b32 m0, s3
	v_readfirstlane_b32 s3, v20
	v_add_u32_e32 v20, 0xa000, v1
	global_load_lds_dwordx4 v[18:19], off
	v_lshl_add_u64 v[18:19], v[4:5], 0, s[10:11]
	s_mov_b32 m0, s3
	v_readfirstlane_b32 s3, v20
	v_add_u32_e32 v20, 0xb000, v1
	global_load_lds_dwordx4 v[18:19], off
	v_lshl_add_u64 v[18:19], v[6:7], 0, s[10:11]
	s_mov_b32 m0, s3
	v_readfirstlane_b32 s3, v20
	v_add_u32_e32 v20, 0xc000, v1
	global_load_lds_dwordx4 v[18:19], off
	v_lshl_add_u64 v[18:19], v[8:9], 0, s[10:11]
	s_mov_b32 m0, s3
	v_readfirstlane_b32 s3, v20
	v_add_u32_e32 v20, 0xd000, v1
	global_load_lds_dwordx4 v[18:19], off
	v_lshl_add_u64 v[18:19], v[10:11], 0, s[10:11]
	s_mov_b32 m0, s3
	v_readfirstlane_b32 s3, v20
	v_add_u32_e32 v20, 0xe000, v1
	global_load_lds_dwordx4 v[18:19], off
	v_lshl_add_u64 v[18:19], v[12:13], 0, s[10:11]
	s_mov_b32 m0, s3
	v_readfirstlane_b32 s3, v20
	v_add_u32_e32 v20, 0xf000, v1
	global_load_lds_dwordx4 v[18:19], off
	v_lshl_add_u64 v[18:19], v[14:15], 0, s[10:11]
	s_mov_b32 m0, s3
	v_readfirstlane_b32 s3, v20
	global_load_lds_dwordx4 v[18:19], off
	v_lshl_add_u64 v[18:19], v[16:17], 0, s[10:11]
	s_mov_b32 m0, s3
	s_cmp_lt_i32 s6, 64
	global_load_lds_dwordx4 v[18:19], off
	s_waitcnt vmcnt(8)
	s_barrier
	s_cbranch_scc1 .LBB3_8
	s_mov_b32 s11, 0
	s_mov_b32 s3, 2
	s_movk_i32 s10, 0x80
	s_mov_b32 s15, s11
	v_readfirstlane_b32 s17, v1
	s_branch .LBB3_4

.LBB3_6:
	s_andn2_b64 vcc, exec, s[12:13]
	s_cbranch_vccnz .LBB3_3
	s_lshl_b32 s16, s3, 15
	s_add_i32 s16, s16, s17
	s_lshl_b64 s[12:13], s[10:11], 1
	s_mov_b32 m0, s16
	v_lshl_add_u64 v[18:19], v[2:3], 0, s[12:13]
	s_add_i32 s16, s16, 0x1000
	global_load_lds_dwordx4 v[18:19], off
	s_mov_b32 m0, s16
	v_lshl_add_u64 v[18:19], v[4:5], 0, s[12:13]
	s_add_i32 s16, s16, 0x1000
	global_load_lds_dwordx4 v[18:19], off
	s_mov_b32 m0, s16
	v_lshl_add_u64 v[18:19], v[6:7], 0, s[12:13]
	s_add_i32 s16, s16, 0x1000
	global_load_lds_dwordx4 v[18:19], off
	s_mov_b32 m0, s16
	v_lshl_add_u64 v[18:19], v[8:9], 0, s[12:13]
	s_add_i32 s16, s16, 0x1000
	global_load_lds_dwordx4 v[18:19], off
	s_mov_b32 m0, s16
	v_lshl_add_u64 v[18:19], v[10:11], 0, s[12:13]
	s_add_i32 s16, s16, 0x1000
	global_load_lds_dwordx4 v[18:19], off
	s_mov_b32 m0, s16
	v_lshl_add_u64 v[18:19], v[12:13], 0, s[12:13]
	s_add_i32 s16, s16, 0x1000
	global_load_lds_dwordx4 v[18:19], off
	s_mov_b32 m0, s16
	v_lshl_add_u64 v[18:19], v[14:15], 0, s[12:13]
	s_add_i32 s16, s16, 0x1000
	global_load_lds_dwordx4 v[18:19], off
	s_mov_b32 m0, s16
	v_lshl_add_u64 v[18:19], v[16:17], 0, s[12:13]
	s_add_i32 s16, s16, 0x1000
	global_load_lds_dwordx4 v[18:19], off
	s_waitcnt vmcnt(8)
	s_barrier
	s_branch .LBB3_3

amdhsa.kernels:
  - .agpr_count:     0
    .args:
      - .actual_access:  read_only
        .address_space:  global
        .offset:         0
        .size:           8
        .value_kind:     global_buffer
      - .actual_access:  read_only
        .address_space:  global
        .offset:         8
        .size:           8
        .value_kind:     global_buffer
      - .actual_access:  read_only
        .address_space:  global
        .offset:         16
        .size:           8
        .value_kind:     global_buffer
      - .actual_access:  read_only
        .address_space:  global
        .offset:         24
        .size:           8
        .value_kind:     global_buffer
      - .actual_access:  read_only
        .address_space:  global
        .offset:         32
        .size:           8
        .value_kind:     global_buffer
      - .address_space:  global
        .offset:         40
        .size:           8
        .value_kind:     global_buffer
      - .address_space:  global
        .offset:         48
        .size:           8
        .value_kind:     global_buffer
      - .address_space:  global
        .offset:         56
        .size:           8
        .value_kind:     global_buffer
      - .address_space:  global
        .offset:         64
        .size:           8
        .value_kind:     global_buffer
    .group_segment_fixed_size: 0
    .kernarg_segment_align: 8
    .kernarg_segment_size: 72
    .language:       OpenCL C
    .language_version:
      - 2
      - 0
    .max_flat_workgroup_size: 256
    .name:           _Z11prep_kernelPKfS0_S0_S0_S0_PDF16_S1_S1_P15HIP_vector_typeIfLj2EE
    .private_segment_fixed_size: 0
    .sgpr_count:     22
    .sgpr_spill_count: 0
    .symbol:         _Z11prep_kernelPKfS0_S0_S0_S0_PDF16_S1_S1_P15HIP_vector_typeIfLj2EE.kd
    .uniform_work_group_size: 1
    .uses_dynamic_stack: false
    .vgpr_count:     20
    .vgpr_spill_count: 0
    .wavefront_size: 64
  - .agpr_count:     0
    .args:
      - .address_space:  global
        .offset:         0
        .size:           8
        .value_kind:     global_buffer
      - .address_space:  global
        .offset:         8
        .size:           8
        .value_kind:     global_buffer
      - .address_space:  global
        .offset:         16
        .size:           8
        .value_kind:     global_buffer
      - .address_space:  global
        .offset:         24
        .size:           8
        .value_kind:     global_buffer
    .group_segment_fixed_size: 0
    .kernarg_segment_align: 8
    .kernarg_segment_size: 32
    .language:       OpenCL C
    .language_version:
      - 2
      - 0
    .max_flat_workgroup_size: 512
    .name:           _Z10attn64_fwdPKDF16_S0_S0_PDF16_
    .private_segment_fixed_size: 0
    .sgpr_count:     48
    .sgpr_spill_count: 0
    .symbol:         _Z10attn64_fwdPKDF16_S0_S0_PDF16_.kd
    .uniform_work_group_size: 1
    .uses_dynamic_stack: false
    .vgpr_count:     252
    .vgpr_spill_count: 0
    .wavefront_size: 64
  - .agpr_count:     0
    .args:
      - .address_space:  global
        .offset:         0
        .size:           8
        .value_kind:     global_buffer
      - .address_space:  global
        .offset:         8
        .size:           8
        .value_kind:     global_buffer
      - .address_space:  global
        .offset:         16
        .size:           8
        .value_kind:     global_buffer
      - .address_space:  global
        .offset:         24
        .size:           8
        .value_kind:     global_buffer
      - .address_space:  global
        .offset:         32
        .size:           8
        .value_kind:     global_buffer
      - .address_space:  global
        .offset:         40
        .size:           8
        .value_kind:     global_buffer
      - .actual_access:  read_only
        .address_space:  global
        .offset:         48
        .size:           8
        .value_kind:     global_buffer
      - .offset:         56
        .size:           4
        .value_kind:     by_value
      - .offset:         60
        .size:           4
        .value_kind:     by_value
      - .offset:         64
        .size:           4
        .value_kind:     by_value
    .group_segment_fixed_size: 32768
    .kernarg_segment_align: 8
    .kernarg_segment_size: 68
    .language:       OpenCL C
    .language_version:
      - 2
      - 0
    .max_flat_workgroup_size: 768
    .name:           _Z7gemm_dbILi256ELi192ELi64ELi96ELi64ELi2ELi1ELi4EEvPKDF16_S1_PfPDF16_S3_S3_PK15HIP_vector_typeIfLj2EEiii
    .private_segment_fixed_size: 0
    .sgpr_count:     27
    .sgpr_spill_count: 0
    .symbol:         _Z7gemm_dbILi256ELi192ELi64ELi96ELi64ELi2ELi1ELi4EEvPKDF16_S1_PfPDF16_S3_S3_PK15HIP_vector_typeIfLj2EEiii.kd
    .uniform_work_group_size: 1
    .uses_dynamic_stack: false
    .vgpr_count:     141
    .vgpr_spill_count: 0
    .wavefront_size: 64
  - .agpr_count:     0
    .args:
      - .address_space:  global
        .offset:         0
        .size:           8
        .value_kind:     global_buffer
      - .address_space:  global
        .offset:         8
        .size:           8
        .value_kind:     global_buffer
      - .address_space:  global
        .offset:         16
        .size:           8
        .value_kind:     global_buffer
      - .address_space:  global
        .offset:         24
        .size:           8
        .value_kind:     global_buffer
      - .address_space:  global
        .offset:         32
        .size:           8
        .value_kind:     global_buffer
      - .address_space:  global
        .offset:         40
        .size:           8
        .value_kind:     global_buffer
      - .actual_access:  read_only
        .address_space:  global
        .offset:         48
        .size:           8
        .value_kind:     global_buffer
      - .offset:         56
        .size:           4
        .value_kind:     by_value
      - .offset:         60
        .size:           4
        .value_kind:     by_value
      - .offset:         64
        .size:           4
        .value_kind:     by_value
    .group_segment_fixed_size: 0
    .kernarg_segment_align: 8
    .kernarg_segment_size: 68
    .language:       OpenCL C
    .language_version:
      - 2
      - 0
    .max_flat_workgroup_size: 512
    .name:           _Z7gemm_dbILi128ELi128ELi64ELi64ELi64ELi3ELi0ELi4EEvPKDF16_S1_PfPDF16_S3_S3_PK15HIP_vector_typeIfLj2EEiii
    .private_segment_fixed_size: 0
    .sgpr_count:     26
    .sgpr_spill_count: 0
    .symbol:         _Z7gemm_dbILi128ELi128ELi64ELi64ELi64ELi3ELi0ELi4EEvPKDF16_S1_PfPDF16_S3_S3_PK15HIP_vector_typeIfLj2EEiii.kd
    .uniform_work_group_size: 1
    .uses_dynamic_stack: false
    .vgpr_count:     168
    .vgpr_spill_count: 0
    .wavefront_size: 64
